# V phase: replaced hipcc's SLP mul/mov/add tree for the channel-6/7 accumulator (last 12 slots of a trip, 60 instr) by 12 v_pk_fma_f32 with op_sel for odd-register weights; f32 accumulation order of th
# speedup vs baseline: 1.0138x; 1.0090x over previous
.LBB0_956:
	s_and_b32 s8, s3, 0x78
	s_add_i32 s8, s8, s4
	s_ashr_i32 s9, s8, 31
	s_lshl_b64 s[10:11], s[8:9], 15
	s_add_u32 s10, s12, s10
	s_addc_u32 s11, s13, s11
	s_and_b32 s17, s16, 0x1000
	s_lshl_b32 s17, s17, 2
	s_add_u32 s10, s10, s17
	s_addc_u32 s11, s11, 0
	v_lshl_add_u64 v[54:55], s[10:11], 0, v[2:3]
	v_lshl_add_u64 v[126:127], v[54:55], 0, s[6:7]
	v_add_co_u32_e32 v128, vcc, s14, v54
	s_mov_b32 s17, s18
	s_nop 0
	v_addc_co_u32_e32 v129, vcc, 0, v55, vcc
	global_load_dword v104, v[126:127], off offset:256
	global_load_dword v106, v[126:127], off offset:512
	global_load_dword v108, v[126:127], off offset:768
	global_load_dword v110, v[126:127], off offset:1024
	global_load_dword v112, v[126:127], off offset:1280
	global_load_dword v114, v[126:127], off offset:1536
	global_load_dword v98, v[126:127], off offset:1792
	global_load_dword v100, v[126:127], off offset:2048
	global_load_dword v116, v[128:129], off offset:-4096
	global_load_dword v102, v[126:127], off offset:2304
	global_load_dword v78, v[126:127], off offset:2560
	global_load_dword v80, v[126:127], off offset:2816
	global_load_dword v82, v[126:127], off offset:3072
	global_load_dword v84, v[126:127], off offset:3328
	global_load_dword v86, v[126:127], off offset:3584
	global_load_dword v88, v[126:127], off offset:3840
	global_load_dword v90, v[128:129], off
	global_load_dword v92, v[128:129], off offset:256
	global_load_dword v94, v[128:129], off offset:512
	global_load_dword v96, v[128:129], off offset:768
	global_load_dword v76, v[128:129], off offset:1024
	global_load_dword v77, v[128:129], off offset:1280
	global_load_dword v56, v[128:129], off offset:1536
	global_load_dword v57, v[128:129], off offset:1792
	global_load_dword v58, v[128:129], off offset:2048
	global_load_dword v59, v[128:129], off offset:2304
	global_load_dword v60, v[128:129], off offset:2560
	global_load_dword v61, v[128:129], off offset:2816
	global_load_dword v62, v[128:129], off offset:3072
	global_load_dword v63, v[128:129], off offset:3328
	global_load_dword v54, v[128:129], off offset:3584
	global_load_dword v55, v[128:129], off offset:3840
	s_waitcnt vmcnt(56)
	v_and_b32_e32 v9, 0x1fff8, v64
	v_and_b32_e32 v11, 0x1fff8, v66
	v_and_b32_e32 v13, 0x1fff8, v68
	v_and_b32_e32 v15, 0x1fff8, v70
	ds_read_b64 v[126:127], v9
	ds_read_b64 v[128:129], v11
	ds_read_b64 v[130:131], v13
	ds_read_b64 v[132:133], v15
	v_and_b32_e32 v9, 0x1fff8, v72
	v_and_b32_e32 v11, 0x1fff8, v74
	v_and_b32_e32 v13, 0x1fff8, v48
	v_and_b32_e32 v15, 0x1fff8, v50
	ds_read_b64 v[134:135], v9
	ds_read_b64 v[136:137], v11
	ds_read_b64 v[138:139], v13
	ds_read_b64 v[140:141], v15
	s_setprio 1
	s_waitcnt lgkmcnt(7)
	v_cvt_pk_f32_fp8_e32 v[142:143], v126
	v_cvt_pk_f32_fp8_sdwa v[144:145], v126 src0_sel:WORD_1
	v_cvt_pk_f32_fp8_e32 v[146:147], v127
	v_cvt_pk_f32_fp8_sdwa v[126:127], v127 src0_sel:WORD_1
	s_waitcnt lgkmcnt(6)
	v_cvt_pk_f32_fp8_e32 v[148:149], v128
	v_cvt_pk_f32_fp8_sdwa v[150:151], v128 src0_sel:WORD_1
	v_cvt_pk_f32_fp8_e32 v[152:153], v129
	v_cvt_pk_f32_fp8_sdwa v[128:129], v129 src0_sel:WORD_1
	s_waitcnt lgkmcnt(5)
	v_cvt_pk_f32_fp8_e32 v[154:155], v130
	v_cvt_pk_f32_fp8_sdwa v[156:157], v130 src0_sel:WORD_1
	v_cvt_pk_f32_fp8_e32 v[158:159], v131
	v_cvt_pk_f32_fp8_sdwa v[130:131], v131 src0_sel:WORD_1
	s_waitcnt lgkmcnt(4)
	v_cvt_pk_f32_fp8_e32 v[160:161], v132
	v_cvt_pk_f32_fp8_sdwa v[162:163], v132 src0_sel:WORD_1
	v_cvt_pk_f32_fp8_e32 v[164:165], v133
	v_cvt_pk_f32_fp8_sdwa v[132:133], v133 src0_sel:WORD_1
	s_waitcnt lgkmcnt(3)
	v_cvt_pk_f32_fp8_e32 v[166:167], v134
	v_cvt_pk_f32_fp8_sdwa v[168:169], v134 src0_sel:WORD_1
	v_cvt_pk_f32_fp8_e32 v[170:171], v135
	v_cvt_pk_f32_fp8_sdwa v[134:135], v135 src0_sel:WORD_1
	s_waitcnt lgkmcnt(2)
	v_cvt_pk_f32_fp8_e32 v[172:173], v136
	v_cvt_pk_f32_fp8_sdwa v[174:175], v136 src0_sel:WORD_1
	v_cvt_pk_f32_fp8_e32 v[176:177], v137
	v_cvt_pk_f32_fp8_sdwa v[136:137], v137 src0_sel:WORD_1
	s_waitcnt lgkmcnt(1)
	v_cvt_pk_f32_fp8_e32 v[178:179], v138
	v_cvt_pk_f32_fp8_sdwa v[180:181], v138 src0_sel:WORD_1
	v_cvt_pk_f32_fp8_e32 v[182:183], v139
	v_cvt_pk_f32_fp8_sdwa v[138:139], v139 src0_sel:WORD_1
	s_waitcnt lgkmcnt(0)
	v_cvt_pk_f32_fp8_e32 v[184:185], v140
	v_cvt_pk_f32_fp8_sdwa v[186:187], v140 src0_sel:WORD_1
	v_cvt_pk_f32_fp8_e32 v[188:189], v141
	v_cvt_pk_f32_fp8_sdwa v[140:141], v141 src0_sel:WORD_1
	s_setprio 0
	s_waitcnt vmcnt(48)
	v_and_b32_e32 v9, 0x1fff8, v52
	v_and_b32_e32 v11, 0x1fff8, v32
	v_and_b32_e32 v13, 0x1fff8, v34
	v_and_b32_e32 v15, 0x1fff8, v36
	ds_read_b64 v[190:191], v9
	ds_read_b64 v[192:193], v11
	ds_read_b64 v[194:195], v13
	ds_read_b64 v[196:197], v15
	v_and_b32_e32 v9, 0x1fff8, v38
	v_and_b32_e32 v11, 0x1fff8, v40
	v_and_b32_e32 v13, 0x1fff8, v42
	v_and_b32_e32 v15, 0x1fff8, v44
	ds_read_b64 v[198:199], v9
	ds_read_b64 v[200:201], v11
	ds_read_b64 v[202:203], v13
	ds_read_b64 v[204:205], v15
	s_setprio 1
	v_pk_fma_f32 v[118:119], v[142:143], v[64:65], v[118:119] op_sel_hi:[1,0,1]
	v_pk_fma_f32 v[122:123], v[144:145], v[64:65], v[122:123] op_sel_hi:[1,0,1]
	v_pk_fma_f32 v[120:121], v[146:147], v[64:65], v[120:121] op_sel_hi:[1,0,1]
	v_pk_fma_f32 v[64:65], v[126:127], v[64:65], v[124:125] op_sel_hi:[1,0,1]
	v_pk_fma_f32 v[118:119], v[148:149], v[66:67], v[118:119] op_sel_hi:[1,0,1]
	v_pk_fma_f32 v[122:123], v[150:151], v[66:67], v[122:123] op_sel_hi:[1,0,1]
	v_pk_fma_f32 v[120:121], v[152:153], v[66:67], v[120:121] op_sel_hi:[1,0,1]
	v_pk_fma_f32 v[64:65], v[128:129], v[66:67], v[64:65] op_sel_hi:[1,0,1]
	v_pk_fma_f32 v[118:119], v[154:155], v[68:69], v[118:119] op_sel_hi:[1,0,1]
	v_pk_fma_f32 v[122:123], v[156:157], v[68:69], v[122:123] op_sel_hi:[1,0,1]
	v_pk_fma_f32 v[120:121], v[158:159], v[68:69], v[120:121] op_sel_hi:[1,0,1]
	v_pk_fma_f32 v[64:65], v[130:131], v[68:69], v[64:65] op_sel_hi:[1,0,1]
	v_pk_fma_f32 v[118:119], v[160:161], v[70:71], v[118:119] op_sel_hi:[1,0,1]
	v_pk_fma_f32 v[122:123], v[162:163], v[70:71], v[122:123] op_sel_hi:[1,0,1]
	v_pk_fma_f32 v[120:121], v[164:165], v[70:71], v[120:121] op_sel_hi:[1,0,1]
	v_pk_fma_f32 v[64:65], v[132:133], v[70:71], v[64:65] op_sel_hi:[1,0,1]
	s_waitcnt lgkmcnt(7)
	v_cvt_pk_f32_fp8_e32 v[206:207], v190
	v_cvt_pk_f32_fp8_sdwa v[208:209], v190 src0_sel:WORD_1
	v_cvt_pk_f32_fp8_e32 v[210:211], v191
	v_cvt_pk_f32_fp8_sdwa v[190:191], v191 src0_sel:WORD_1
	v_pk_fma_f32 v[118:119], v[166:167], v[72:73], v[118:119] op_sel_hi:[1,0,1]
	v_pk_fma_f32 v[122:123], v[168:169], v[72:73], v[122:123] op_sel_hi:[1,0,1]
	v_pk_fma_f32 v[120:121], v[170:171], v[72:73], v[120:121] op_sel_hi:[1,0,1]
	v_pk_fma_f32 v[64:65], v[134:135], v[72:73], v[64:65] op_sel_hi:[1,0,1]
	v_pk_fma_f32 v[118:119], v[172:173], v[74:75], v[118:119] op_sel_hi:[1,0,1]
	v_pk_fma_f32 v[122:123], v[174:175], v[74:75], v[122:123] op_sel_hi:[1,0,1]
	v_pk_fma_f32 v[120:121], v[176:177], v[74:75], v[120:121] op_sel_hi:[1,0,1]
	v_pk_fma_f32 v[64:65], v[136:137], v[74:75], v[64:65] op_sel_hi:[1,0,1]
	s_waitcnt lgkmcnt(6)
	v_cvt_pk_f32_fp8_e32 v[66:67], v192
	v_cvt_pk_f32_fp8_sdwa v[68:69], v192 src0_sel:WORD_1
	v_cvt_pk_f32_fp8_e32 v[70:71], v193
	v_cvt_pk_f32_fp8_sdwa v[72:73], v193 src0_sel:WORD_1
	s_waitcnt lgkmcnt(5)
	v_cvt_pk_f32_fp8_e32 v[74:75], v194
	v_cvt_pk_f32_fp8_sdwa v[124:125], v194 src0_sel:WORD_1
	v_pk_fma_f32 v[118:119], v[178:179], v[48:49], v[118:119] op_sel_hi:[1,0,1]
	v_pk_fma_f32 v[122:123], v[180:181], v[48:49], v[122:123] op_sel_hi:[1,0,1]
	v_pk_fma_f32 v[120:121], v[182:183], v[48:49], v[120:121] op_sel_hi:[1,0,1]
	v_pk_fma_f32 v[48:49], v[138:139], v[48:49], v[64:65] op_sel_hi:[1,0,1]
	v_pk_fma_f32 v[118:119], v[184:185], v[50:51], v[118:119] op_sel_hi:[1,0,1]
	v_pk_fma_f32 v[122:123], v[186:187], v[50:51], v[122:123] op_sel_hi:[1,0,1]
	v_pk_fma_f32 v[120:121], v[188:189], v[50:51], v[120:121] op_sel_hi:[1,0,1]
	v_pk_fma_f32 v[48:49], v[140:141], v[50:51], v[48:49] op_sel_hi:[1,0,1]
	v_pk_fma_f32 v[118:119], v[206:207], v[52:53], v[118:119] op_sel_hi:[1,0,1]
	v_pk_fma_f32 v[122:123], v[208:209], v[52:53], v[122:123] op_sel_hi:[1,0,1]
	v_pk_fma_f32 v[120:121], v[210:211], v[52:53], v[120:121] op_sel_hi:[1,0,1]
	v_pk_fma_f32 v[48:49], v[190:191], v[52:53], v[48:49] op_sel_hi:[1,0,1]
	v_cvt_pk_f32_fp8_e32 v[126:127], v195
	v_cvt_pk_f32_fp8_sdwa v[128:129], v195 src0_sel:WORD_1
	s_waitcnt lgkmcnt(4)
	v_cvt_pk_f32_fp8_e32 v[130:131], v196
	v_cvt_pk_f32_fp8_sdwa v[132:133], v196 src0_sel:WORD_1
	v_cvt_pk_f32_fp8_e32 v[134:135], v197
	v_cvt_pk_f32_fp8_sdwa v[136:137], v197 src0_sel:WORD_1
	s_waitcnt lgkmcnt(3)
	v_cvt_pk_f32_fp8_e32 v[142:143], v198
	v_cvt_pk_f32_fp8_sdwa v[144:145], v198 src0_sel:WORD_1
	v_cvt_pk_f32_fp8_e32 v[146:147], v199
	v_cvt_pk_f32_fp8_sdwa v[148:149], v199 src0_sel:WORD_1
	s_waitcnt lgkmcnt(2)
	v_cvt_pk_f32_fp8_e32 v[150:151], v200
	v_cvt_pk_f32_fp8_sdwa v[152:153], v200 src0_sel:WORD_1
	v_cvt_pk_f32_fp8_e32 v[154:155], v201
	v_cvt_pk_f32_fp8_sdwa v[156:157], v201 src0_sel:WORD_1
	s_waitcnt lgkmcnt(1)
	v_cvt_pk_f32_fp8_e32 v[158:159], v202
	v_cvt_pk_f32_fp8_sdwa v[160:161], v202 src0_sel:WORD_1
	v_cvt_pk_f32_fp8_e32 v[162:163], v203
	v_cvt_pk_f32_fp8_sdwa v[164:165], v203 src0_sel:WORD_1
	s_waitcnt lgkmcnt(0)
	v_cvt_pk_f32_fp8_e32 v[166:167], v204
	v_cvt_pk_f32_fp8_sdwa v[168:169], v204 src0_sel:WORD_1
	v_cvt_pk_f32_fp8_e32 v[170:171], v205
	v_cvt_pk_f32_fp8_sdwa v[172:173], v205 src0_sel:WORD_1
	s_setprio 0
	s_waitcnt vmcnt(40)
	v_and_b32_e32 v9, 0x1fff8, v46
	v_and_b32_e32 v11, 0x1fff8, v26
	v_and_b32_e32 v13, 0x1fff8, v28
	v_and_b32_e32 v15, 0x1fff8, v30
	ds_read_b64 v[50:51], v9
	ds_read_b64 v[52:53], v11
	ds_read_b64 v[64:65], v13
	ds_read_b64 v[138:139], v15
	v_and_b32_e32 v9, 0x1fff8, v4
	v_and_b32_e32 v11, 0x1fff8, v6
	v_and_b32_e32 v13, 0x1fff8, v8
	v_and_b32_e32 v15, 0x1fff8, v10
	ds_read_b64 v[140:141], v9
	ds_read_b64 v[174:175], v11
	ds_read_b64 v[176:177], v13
	ds_read_b64 v[178:179], v15
	s_setprio 1
	v_pk_fma_f32 v[66:67], v[66:67], v[32:33], v[118:119] op_sel_hi:[1,0,1]
	v_pk_fma_f32 v[68:69], v[68:69], v[32:33], v[122:123] op_sel_hi:[1,0,1]
	v_pk_fma_f32 v[70:71], v[70:71], v[32:33], v[120:121] op_sel_hi:[1,0,1]
	v_pk_fma_f32 v[32:33], v[72:73], v[32:33], v[48:49] op_sel_hi:[1,0,1]
	v_pk_fma_f32 v[66:67], v[74:75], v[34:35], v[66:67] op_sel_hi:[1,0,1]
	v_pk_fma_f32 v[68:69], v[124:125], v[34:35], v[68:69] op_sel_hi:[1,0,1]
	v_pk_fma_f32 v[70:71], v[126:127], v[34:35], v[70:71] op_sel_hi:[1,0,1]
	v_pk_fma_f32 v[32:33], v[128:129], v[34:35], v[32:33] op_sel_hi:[1,0,1]
	v_pk_fma_f32 v[66:67], v[130:131], v[36:37], v[66:67] op_sel_hi:[1,0,1]
	v_pk_fma_f32 v[68:69], v[132:133], v[36:37], v[68:69] op_sel_hi:[1,0,1]
	v_pk_fma_f32 v[70:71], v[134:135], v[36:37], v[70:71] op_sel_hi:[1,0,1]
	v_pk_fma_f32 v[32:33], v[136:137], v[36:37], v[32:33] op_sel_hi:[1,0,1]
	s_waitcnt lgkmcnt(7)
	v_cvt_pk_f32_fp8_e32 v[180:181], v50
	v_cvt_pk_f32_fp8_sdwa v[182:183], v50 src0_sel:WORD_1
	v_cvt_pk_f32_fp8_e32 v[184:185], v51
	v_cvt_pk_f32_fp8_sdwa v[50:51], v51 src0_sel:WORD_1
	v_pk_fma_f32 v[66:67], v[142:143], v[38:39], v[66:67] op_sel_hi:[1,0,1]
	v_pk_fma_f32 v[68:69], v[144:145], v[38:39], v[68:69] op_sel_hi:[1,0,1]
	v_pk_fma_f32 v[70:71], v[146:147], v[38:39], v[70:71] op_sel_hi:[1,0,1]
	v_pk_fma_f32 v[32:33], v[148:149], v[38:39], v[32:33] op_sel_hi:[1,0,1]
	s_waitcnt lgkmcnt(6)
	v_cvt_pk_f32_fp8_e32 v[186:187], v52
	v_cvt_pk_f32_fp8_sdwa v[188:189], v52 src0_sel:WORD_1
	v_cvt_pk_f32_fp8_e32 v[190:191], v53
	v_cvt_pk_f32_fp8_sdwa v[52:53], v53 src0_sel:WORD_1
	v_pk_fma_f32 v[66:67], v[150:151], v[40:41], v[66:67] op_sel_hi:[1,0,1]
	v_pk_fma_f32 v[68:69], v[152:153], v[40:41], v[68:69] op_sel_hi:[1,0,1]
	v_pk_fma_f32 v[70:71], v[154:155], v[40:41], v[70:71] op_sel_hi:[1,0,1]
	v_pk_fma_f32 v[32:33], v[156:157], v[40:41], v[32:33] op_sel_hi:[1,0,1]
	s_waitcnt lgkmcnt(5)
	v_cvt_pk_f32_fp8_e32 v[192:193], v64
	v_cvt_pk_f32_fp8_sdwa v[194:195], v64 src0_sel:WORD_1
	v_cvt_pk_f32_fp8_e32 v[196:197], v65
	v_cvt_pk_f32_fp8_sdwa v[64:65], v65 src0_sel:WORD_1
	v_pk_fma_f32 v[66:67], v[158:159], v[42:43], v[66:67] op_sel_hi:[1,0,1]
	v_pk_fma_f32 v[68:69], v[160:161], v[42:43], v[68:69] op_sel_hi:[1,0,1]
	v_pk_fma_f32 v[70:71], v[162:163], v[42:43], v[70:71] op_sel_hi:[1,0,1]
	v_pk_fma_f32 v[32:33], v[164:165], v[42:43], v[32:33] op_sel_hi:[1,0,1]
	s_waitcnt lgkmcnt(4)
	v_cvt_pk_f32_fp8_e32 v[198:199], v138
	v_cvt_pk_f32_fp8_sdwa v[200:201], v138 src0_sel:WORD_1
	v_cvt_pk_f32_fp8_e32 v[202:203], v139
	v_cvt_pk_f32_fp8_sdwa v[138:139], v139 src0_sel:WORD_1
	v_pk_fma_f32 v[66:67], v[166:167], v[44:45], v[66:67] op_sel_hi:[1,0,1]
	v_pk_fma_f32 v[68:69], v[168:169], v[44:45], v[68:69] op_sel_hi:[1,0,1]
	v_pk_fma_f32 v[70:71], v[170:171], v[44:45], v[70:71] op_sel_hi:[1,0,1]
	v_pk_fma_f32 v[32:33], v[172:173], v[44:45], v[32:33] op_sel_hi:[1,0,1]
	v_pk_fma_f32 v[66:67], v[180:181], v[46:47], v[66:67] op_sel_hi:[1,0,1]
	v_pk_fma_f32 v[68:69], v[182:183], v[46:47], v[68:69] op_sel_hi:[1,0,1]
	v_pk_fma_f32 v[70:71], v[184:185], v[46:47], v[70:71] op_sel_hi:[1,0,1]
	v_pk_fma_f32 v[32:33], v[50:51], v[46:47], v[32:33] op_sel_hi:[1,0,1]
	s_waitcnt lgkmcnt(3)
	v_cvt_pk_f32_fp8_e32 v[34:35], v140
	v_cvt_pk_f32_fp8_sdwa v[36:37], v140 src0_sel:WORD_1
	v_cvt_pk_f32_fp8_e32 v[38:39], v141
	v_cvt_pk_f32_fp8_sdwa v[40:41], v141 src0_sel:WORD_1
	s_waitcnt lgkmcnt(2)
	v_cvt_pk_f32_fp8_e32 v[42:43], v174
	v_cvt_pk_f32_fp8_sdwa v[44:45], v174 src0_sel:WORD_1
	v_cvt_pk_f32_fp8_e32 v[46:47], v175
	v_cvt_pk_f32_fp8_sdwa v[48:49], v175 src0_sel:WORD_1
	s_waitcnt lgkmcnt(1)
	v_cvt_pk_f32_fp8_e32 v[50:51], v176
	v_cvt_pk_f32_fp8_sdwa v[72:73], v176 src0_sel:WORD_1
	v_cvt_pk_f32_fp8_e32 v[74:75], v177
	v_cvt_pk_f32_fp8_sdwa v[118:119], v177 src0_sel:WORD_1
	s_waitcnt lgkmcnt(0)
	v_cvt_pk_f32_fp8_e32 v[120:121], v178
	v_cvt_pk_f32_fp8_sdwa v[122:123], v178 src0_sel:WORD_1
	v_cvt_pk_f32_fp8_e32 v[124:125], v179
	v_pk_fma_f32 v[66:67], v[186:187], v[26:27], v[66:67] op_sel_hi:[1,0,1]
	v_pk_fma_f32 v[68:69], v[188:189], v[26:27], v[68:69] op_sel_hi:[1,0,1]
	v_pk_fma_f32 v[70:71], v[190:191], v[26:27], v[70:71] op_sel_hi:[1,0,1]
	v_pk_fma_f32 v[26:27], v[52:53], v[26:27], v[32:33] op_sel_hi:[1,0,1]
	v_pk_fma_f32 v[66:67], v[192:193], v[28:29], v[66:67] op_sel_hi:[1,0,1]
	v_pk_fma_f32 v[68:69], v[194:195], v[28:29], v[68:69] op_sel_hi:[1,0,1]
	v_pk_fma_f32 v[70:71], v[196:197], v[28:29], v[70:71] op_sel_hi:[1,0,1]
	v_pk_fma_f32 v[26:27], v[64:65], v[28:29], v[26:27] op_sel_hi:[1,0,1]
	v_pk_fma_f32 v[66:67], v[198:199], v[30:31], v[66:67] op_sel_hi:[1,0,1]
	v_pk_fma_f32 v[68:69], v[200:201], v[30:31], v[68:69] op_sel_hi:[1,0,1]
	v_pk_fma_f32 v[70:71], v[202:203], v[30:31], v[70:71] op_sel_hi:[1,0,1]
	v_pk_fma_f32 v[26:27], v[138:139], v[30:31], v[26:27] op_sel_hi:[1,0,1]
	v_cvt_pk_f32_fp8_sdwa v[126:127], v179 src0_sel:WORD_1
	s_setprio 0
	s_waitcnt vmcnt(32)
	v_and_b32_e32 v9, 0x1fff8, v14
	v_and_b32_e32 v11, 0x1fff8, v18
	v_and_b32_e32 v13, 0x1fff8, v20
	v_and_b32_e32 v15, 0x1fff8, v22
	ds_read_b64 v[28:29], v9
	ds_read_b64 v[30:31], v11
	ds_read_b64 v[32:33], v13
	ds_read_b64 v[52:53], v15
	v_and_b32_e32 v9, 0x1fff8, v24
	v_and_b32_e32 v11, 0x1fff8, v12
	v_and_b32_e32 v13, 0x1fff8, v16
	v_and_b32_e32 v15, 0x1fff8, v7
	ds_read_b64 v[64:65], v9
	ds_read_b64 v[128:129], v11
	ds_read_b64 v[130:131], v13
	ds_read_b64 v[132:133], v15
	s_setprio 1
	s_waitcnt lgkmcnt(7)
	v_cvt_pk_f32_fp8_e32 v[134:135], v28
	v_pk_fma_f32 v[34:35], v[34:35], v[4:5], v[66:67] op_sel_hi:[1,0,1]
	s_waitcnt lgkmcnt(6)
	v_cvt_pk_f32_fp8_e32 v[140:141], v30
	v_pk_fma_f32 v[34:35], v[42:43], v[6:7], v[34:35] op_sel_hi:[1,0,1]
	s_waitcnt lgkmcnt(5)
	v_cvt_pk_f32_fp8_e32 v[146:147], v32
	v_pk_fma_f32 v[34:35], v[50:51], v[8:9], v[34:35] op_sel_hi:[1,0,1]
	s_waitcnt lgkmcnt(4)
	v_cvt_pk_f32_fp8_e32 v[152:153], v52
	v_pk_fma_f32 v[34:35], v[120:121], v[10:11], v[34:35] op_sel_hi:[1,0,1]
	s_waitcnt lgkmcnt(3)
	v_cvt_pk_f32_fp8_e32 v[158:159], v64
	v_pk_fma_f32 v[34:35], v[134:135], v[14:15], v[34:35] op_sel_hi:[1,0,1]
	s_waitcnt lgkmcnt(2)
	v_cvt_pk_f32_fp8_e32 v[164:165], v128
	v_pk_fma_f32 v[34:35], v[140:141], v[18:19], v[34:35] op_sel_hi:[1,0,1]
	s_waitcnt lgkmcnt(1)
	v_cvt_pk_f32_fp8_e32 v[170:171], v130
	v_pk_fma_f32 v[34:35], v[146:147], v[20:21], v[34:35] op_sel_hi:[1,0,1]
	v_cvt_pk_f32_fp8_sdwa v[136:137], v28 src0_sel:WORD_1
	v_pk_fma_f32 v[34:35], v[152:153], v[22:23], v[34:35] op_sel_hi:[1,0,1]
	v_cvt_pk_f32_fp8_sdwa v[142:143], v30 src0_sel:WORD_1
	v_pk_fma_f32 v[34:35], v[158:159], v[24:25], v[34:35] op_sel_hi:[1,0,1]
	v_cvt_pk_f32_fp8_sdwa v[148:149], v32 src0_sel:WORD_1
	v_pk_fma_f32 v[34:35], v[164:165], v[12:13], v[34:35] op_sel_hi:[1,0,1]
	v_cvt_pk_f32_fp8_sdwa v[154:155], v52 src0_sel:WORD_1
	v_pk_fma_f32 v[120:121], v[170:171], v[16:17], v[34:35] op_sel_hi:[1,0,1]
	v_pk_fma_f32 v[34:35], v[36:37], v[4:5], v[68:69] op_sel_hi:[1,0,1]
	v_cvt_pk_f32_fp8_sdwa v[160:161], v64 src0_sel:WORD_1
	v_pk_fma_f32 v[34:35], v[44:45], v[6:7], v[34:35] op_sel_hi:[1,0,1]
	v_cvt_pk_f32_fp8_sdwa v[166:167], v128 src0_sel:WORD_1
	v_pk_fma_f32 v[34:35], v[72:73], v[8:9], v[34:35] op_sel_hi:[1,0,1]
	v_cvt_pk_f32_fp8_sdwa v[172:173], v130 src0_sel:WORD_1
	v_pk_fma_f32 v[34:35], v[122:123], v[10:11], v[34:35] op_sel_hi:[1,0,1]
	v_cvt_pk_f32_fp8_e32 v[138:139], v29
	v_pk_fma_f32 v[34:35], v[136:137], v[14:15], v[34:35] op_sel_hi:[1,0,1]
	v_cvt_pk_f32_fp8_sdwa v[28:29], v29 src0_sel:WORD_1
	v_pk_fma_f32 v[34:35], v[142:143], v[18:19], v[34:35] op_sel_hi:[1,0,1]
	v_cvt_pk_f32_fp8_e32 v[144:145], v31
	v_pk_fma_f32 v[34:35], v[148:149], v[20:21], v[34:35] op_sel_hi:[1,0,1]
	v_pk_fma_f32 v[26:27], v[40:41], v[4:5], v[26:27] op_sel_hi:[1,0,1]
	v_pk_fma_f32 v[34:35], v[154:155], v[22:23], v[34:35] op_sel_hi:[1,0,1]
	v_cvt_pk_f32_fp8_sdwa v[30:31], v31 src0_sel:WORD_1
	v_pk_fma_f32 v[34:35], v[160:161], v[24:25], v[34:35] op_sel_hi:[1,0,1]
	v_cvt_pk_f32_fp8_e32 v[150:151], v33
	v_pk_fma_f32 v[34:35], v[166:167], v[12:13], v[34:35] op_sel_hi:[1,0,1]
	v_pk_fma_f32 v[26:27], v[48:49], v[6:7], v[26:27] op_sel_hi:[1,0,1]
	v_pk_fma_f32 v[122:123], v[172:173], v[16:17], v[34:35] op_sel_hi:[1,0,1]
	v_pk_fma_f32 v[34:35], v[38:39], v[4:5], v[70:71] op_sel_hi:[1,0,1]
	v_cvt_pk_f32_fp8_sdwa v[32:33], v33 src0_sel:WORD_1
	v_pk_fma_f32 v[34:35], v[46:47], v[6:7], v[34:35] op_sel_hi:[1,0,1]
	v_cvt_pk_f32_fp8_e32 v[156:157], v53
	v_pk_fma_f32 v[34:35], v[74:75], v[8:9], v[34:35] op_sel_hi:[1,0,1]
	v_pk_fma_f32 v[8:9], v[118:119], v[8:9], v[26:27] op_sel_hi:[1,0,1]
	v_pk_fma_f32 v[34:35], v[124:125], v[10:11], v[34:35] op_sel_hi:[1,0,1]
	v_cvt_pk_f32_fp8_sdwa v[52:53], v53 src0_sel:WORD_1
	v_cvt_pk_f32_fp8_e32 v[162:163], v65
	v_pk_fma_f32 v[34:35], v[138:139], v[14:15], v[34:35] op_sel_hi:[1,0,1]
	v_pk_fma_f32 v[8:9], v[126:127], v[10:11], v[8:9] op_sel_hi:[1,0,1]
	v_cvt_pk_f32_fp8_sdwa v[64:65], v65 src0_sel:WORD_1
	v_cvt_pk_f32_fp8_e32 v[168:169], v129
	v_pk_fma_f32 v[34:35], v[144:145], v[18:19], v[34:35] op_sel_hi:[1,0,1]
	v_pk_fma_f32 v[8:9], v[28:29], v[14:15], v[8:9] op_sel_hi:[1,0,1]
	v_cvt_pk_f32_fp8_sdwa v[128:129], v129 src0_sel:WORD_1
	v_cvt_pk_f32_fp8_e32 v[174:175], v131
	v_pk_fma_f32 v[34:35], v[150:151], v[20:21], v[34:35] op_sel_hi:[1,0,1]
	v_pk_fma_f32 v[8:9], v[30:31], v[18:19], v[8:9] op_sel_hi:[1,0,1]
	v_cvt_pk_f32_fp8_sdwa v[130:131], v131 src0_sel:WORD_1
	v_pk_fma_f32 v[34:35], v[156:157], v[22:23], v[34:35] op_sel_hi:[1,0,1]
	v_pk_fma_f32 v[8:9], v[32:33], v[20:21], v[8:9] op_sel_hi:[1,0,1]
	s_waitcnt lgkmcnt(0)
	v_cvt_pk_f32_fp8_e32 v[118:119], v132
	v_pk_fma_f32 v[34:35], v[162:163], v[24:25], v[34:35] op_sel_hi:[1,0,1]
	v_pk_fma_f32 v[8:9], v[52:53], v[22:23], v[8:9] op_sel_hi:[1,0,1]
	v_pk_fma_f32 v[34:35], v[168:169], v[12:13], v[34:35] op_sel_hi:[1,0,1]
	v_pk_fma_f32 v[8:9], v[64:65], v[24:25], v[8:9] op_sel_hi:[1,0,1]
	v_pk_fma_f32 v[124:125], v[174:175], v[16:17], v[34:35] op_sel_hi:[1,0,1]
	v_pk_fma_f32 v[8:9], v[128:129], v[12:13], v[8:9] op_sel_hi:[1,0,1]
	v_cvt_pk_f32_fp8_sdwa v[126:127], v132 src0_sel:WORD_1
	v_cvt_pk_f32_fp8_e32 v[134:135], v133
	v_cvt_pk_f32_fp8_sdwa v[132:133], v133 src0_sel:WORD_1
	v_pk_fma_f32 v[128:129], v[130:131], v[16:17], v[8:9] op_sel_hi:[1,0,1]
	v_mov_b32_e32 v130, v7
	s_setprio 0
	s_add_i32 s18, s18, 2
	s_cmp_gt_u32 s17, 61
	s_cselect_b64 s[10:11], -1, 0
	s_cmp_lt_u32 s17, 62
	s_cselect_b32 s19, s18, 63
	s_lshl_b32 s20, s19, 1
	s_and_b32 s20, s20, 0xf8
	s_add_i32 s20, s20, s4
	s_ashr_i32 s21, s20, 31
	s_lshl_b64 s[20:21], s[20:21], 15
	s_add_u32 s20, s12, s20
	s_addc_u32 s21, s13, s21
	s_lshl_b32 s19, s19, 13
	s_and_b32 s19, s19, 0x6000
	s_add_u32 s20, s20, s19
	s_addc_u32 s21, s21, 0
	v_lshl_add_u64 v[6:7], s[20:21], 0, v[2:3]
	v_add_co_u32_e32 v136, vcc, s5, v6
	global_load_dword v64, v[6:7], off
	global_load_dword v66, v[6:7], off offset:256
	global_load_dword v68, v[6:7], off offset:512
	global_load_dword v70, v[6:7], off offset:768
	global_load_dword v72, v[6:7], off offset:1024
	global_load_dword v74, v[6:7], off offset:1280
	global_load_dword v48, v[6:7], off offset:1536
	global_load_dword v50, v[6:7], off offset:1792
	global_load_dword v52, v[6:7], off offset:2048
	global_load_dword v32, v[6:7], off offset:2304
	global_load_dword v34, v[6:7], off offset:2560
	global_load_dword v36, v[6:7], off offset:2816
	global_load_dword v38, v[6:7], off offset:3072
	global_load_dword v40, v[6:7], off offset:3328
	global_load_dword v42, v[6:7], off offset:3584
	global_load_dword v44, v[6:7], off offset:3840
	v_addc_co_u32_e32 v137, vcc, 0, v7, vcc
	global_load_dword v46, v[136:137], off
	global_load_dword v26, v[136:137], off offset:256
	global_load_dword v28, v[136:137], off offset:512
	global_load_dword v30, v[136:137], off offset:768
	global_load_dword v4, v[136:137], off offset:1024
	global_load_dword v6, v[136:137], off offset:1280
	global_load_dword v8, v[136:137], off offset:1536
	global_load_dword v10, v[136:137], off offset:1792
	global_load_dword v14, v[136:137], off offset:2048
	global_load_dword v18, v[136:137], off offset:2304
	global_load_dword v20, v[136:137], off offset:2560
	global_load_dword v22, v[136:137], off offset:2816
	global_load_dword v24, v[136:137], off offset:3072
	global_load_dword v12, v[136:137], off offset:3328
	global_load_dword v16, v[136:137], off offset:3584
	global_load_dword v7, v[136:137], off offset:3840
	s_waitcnt vmcnt(55)
	v_and_b32_e32 v9, 0x1fff8, v116
	v_and_b32_e32 v11, 0x1fff8, v104
	v_and_b32_e32 v13, 0x1fff8, v106
	v_and_b32_e32 v15, 0x1fff8, v108
	ds_read_b64 v[136:137], v9
	ds_read_b64 v[138:139], v11
	ds_read_b64 v[140:141], v13
	ds_read_b64 v[142:143], v15
	v_and_b32_e32 v9, 0x1fff8, v110
	v_and_b32_e32 v11, 0x1fff8, v112
	v_and_b32_e32 v13, 0x1fff8, v114
	v_and_b32_e32 v15, 0x1fff8, v98
	ds_read_b64 v[144:145], v9
	ds_read_b64 v[146:147], v11
	ds_read_b64 v[148:149], v13
	ds_read_b64 v[150:151], v15
	s_setprio 1
	s_waitcnt lgkmcnt(7)
	v_cvt_pk_f32_fp8_e32 v[152:153], v136
	v_cvt_pk_f32_fp8_sdwa v[154:155], v136 src0_sel:WORD_1
	v_cvt_pk_f32_fp8_e32 v[156:157], v137
	v_cvt_pk_f32_fp8_sdwa v[136:137], v137 src0_sel:WORD_1
	s_waitcnt lgkmcnt(6)
	v_cvt_pk_f32_fp8_e32 v[158:159], v138
	v_cvt_pk_f32_fp8_sdwa v[160:161], v138 src0_sel:WORD_1
	v_cvt_pk_f32_fp8_e32 v[162:163], v139
	v_cvt_pk_f32_fp8_sdwa v[138:139], v139 src0_sel:WORD_1
	s_waitcnt lgkmcnt(5)
	v_cvt_pk_f32_fp8_e32 v[164:165], v140
	v_cvt_pk_f32_fp8_sdwa v[166:167], v140 src0_sel:WORD_1
	v_cvt_pk_f32_fp8_e32 v[168:169], v141
	v_cvt_pk_f32_fp8_sdwa v[140:141], v141 src0_sel:WORD_1
	s_waitcnt lgkmcnt(4)
	v_cvt_pk_f32_fp8_e32 v[170:171], v142
	v_cvt_pk_f32_fp8_sdwa v[172:173], v142 src0_sel:WORD_1
	v_cvt_pk_f32_fp8_e32 v[174:175], v143
	v_cvt_pk_f32_fp8_sdwa v[142:143], v143 src0_sel:WORD_1
	s_waitcnt lgkmcnt(3)
	v_cvt_pk_f32_fp8_e32 v[176:177], v144
	v_cvt_pk_f32_fp8_sdwa v[178:179], v144 src0_sel:WORD_1
	v_cvt_pk_f32_fp8_e32 v[180:181], v145
	v_cvt_pk_f32_fp8_sdwa v[144:145], v145 src0_sel:WORD_1
	s_waitcnt lgkmcnt(2)
	v_cvt_pk_f32_fp8_e32 v[182:183], v146
	v_cvt_pk_f32_fp8_sdwa v[184:185], v146 src0_sel:WORD_1
	v_cvt_pk_f32_fp8_e32 v[186:187], v147
	v_cvt_pk_f32_fp8_sdwa v[146:147], v147 src0_sel:WORD_1
	s_waitcnt lgkmcnt(1)
	v_cvt_pk_f32_fp8_e32 v[188:189], v148
	v_cvt_pk_f32_fp8_sdwa v[190:191], v148 src0_sel:WORD_1
	v_cvt_pk_f32_fp8_e32 v[192:193], v149
	v_cvt_pk_f32_fp8_sdwa v[148:149], v149 src0_sel:WORD_1
	s_waitcnt lgkmcnt(0)
	v_cvt_pk_f32_fp8_e32 v[194:195], v150
	v_cvt_pk_f32_fp8_sdwa v[196:197], v150 src0_sel:WORD_1
	v_cvt_pk_f32_fp8_e32 v[198:199], v151
	v_cvt_pk_f32_fp8_sdwa v[150:151], v151 src0_sel:WORD_1
	s_setprio 0
	v_and_b32_e32 v9, 0x1fff8, v100
	s_waitcnt vmcnt(48)
	v_and_b32_e32 v11, 0x1fff8, v102
	v_and_b32_e32 v13, 0x1fff8, v78
	v_and_b32_e32 v15, 0x1fff8, v80
	ds_read_b64 v[200:201], v9
	ds_read_b64 v[202:203], v11
	ds_read_b64 v[204:205], v13
	ds_read_b64 v[206:207], v15
	v_and_b32_e32 v9, 0x1fff8, v82
	v_and_b32_e32 v11, 0x1fff8, v84
	v_and_b32_e32 v13, 0x1fff8, v86
	v_and_b32_e32 v15, 0x1fff8, v88
	ds_read_b64 v[208:209], v9
	ds_read_b64 v[210:211], v11
	ds_read_b64 v[212:213], v13
	ds_read_b64 v[214:215], v15
	s_setprio 1
	v_pk_fma_f32 v[118:119], v[118:119], v[130:131], v[120:121] op_sel_hi:[1,0,1]
	v_pk_fma_f32 v[120:121], v[126:127], v[130:131], v[122:123] op_sel_hi:[1,0,1]
	v_pk_fma_f32 v[122:123], v[134:135], v[130:131], v[124:125] op_sel_hi:[1,0,1]
	v_pk_fma_f32 v[118:119], v[152:153], v[116:117], v[118:119] op_sel_hi:[1,0,1]
	v_pk_fma_f32 v[120:121], v[154:155], v[116:117], v[120:121] op_sel_hi:[1,0,1]
	v_pk_fma_f32 v[122:123], v[156:157], v[116:117], v[122:123] op_sel_hi:[1,0,1]
	v_pk_fma_f32 v[124:125], v[132:133], v[130:131], v[128:129] op_sel_hi:[1,0,1]
	v_pk_fma_f32 v[118:119], v[158:159], v[104:105], v[118:119] op_sel_hi:[1,0,1]
	v_pk_fma_f32 v[120:121], v[160:161], v[104:105], v[120:121] op_sel_hi:[1,0,1]
	v_pk_fma_f32 v[122:123], v[162:163], v[104:105], v[122:123] op_sel_hi:[1,0,1]
	v_pk_fma_f32 v[116:117], v[136:137], v[116:117], v[124:125] op_sel_hi:[1,0,1]
	v_pk_fma_f32 v[118:119], v[164:165], v[106:107], v[118:119] op_sel_hi:[1,0,1]
	v_pk_fma_f32 v[120:121], v[166:167], v[106:107], v[120:121] op_sel_hi:[1,0,1]
	v_pk_fma_f32 v[122:123], v[168:169], v[106:107], v[122:123] op_sel_hi:[1,0,1]
	v_pk_fma_f32 v[104:105], v[138:139], v[104:105], v[116:117] op_sel_hi:[1,0,1]
	v_pk_fma_f32 v[118:119], v[170:171], v[108:109], v[118:119] op_sel_hi:[1,0,1]
	v_pk_fma_f32 v[120:121], v[172:173], v[108:109], v[120:121] op_sel_hi:[1,0,1]
	v_pk_fma_f32 v[122:123], v[174:175], v[108:109], v[122:123] op_sel_hi:[1,0,1]
	v_pk_fma_f32 v[104:105], v[140:141], v[106:107], v[104:105] op_sel_hi:[1,0,1]
	s_waitcnt lgkmcnt(7)
	v_cvt_pk_f32_fp8_e32 v[216:217], v200
	v_cvt_pk_f32_fp8_sdwa v[218:219], v200 src0_sel:WORD_1
	v_cvt_pk_f32_fp8_e32 v[220:221], v201
	v_pk_fma_f32 v[118:119], v[176:177], v[110:111], v[118:119] op_sel_hi:[1,0,1]
	v_pk_fma_f32 v[120:121], v[178:179], v[110:111], v[120:121] op_sel_hi:[1,0,1]
	v_pk_fma_f32 v[122:123], v[180:181], v[110:111], v[122:123] op_sel_hi:[1,0,1]
	v_pk_fma_f32 v[104:105], v[142:143], v[108:109], v[104:105] op_sel_hi:[1,0,1]
	v_cvt_pk_f32_fp8_sdwa v[200:201], v201 src0_sel:WORD_1
	s_waitcnt lgkmcnt(6)
	v_cvt_pk_f32_fp8_e32 v[222:223], v202
	v_cvt_pk_f32_fp8_sdwa v[224:225], v202 src0_sel:WORD_1
	v_cvt_pk_f32_fp8_e32 v[226:227], v203
	v_pk_fma_f32 v[118:119], v[182:183], v[112:113], v[118:119] op_sel_hi:[1,0,1]
	v_pk_fma_f32 v[120:121], v[184:185], v[112:113], v[120:121] op_sel_hi:[1,0,1]
	v_pk_fma_f32 v[122:123], v[186:187], v[112:113], v[122:123] op_sel_hi:[1,0,1]
	v_pk_fma_f32 v[104:105], v[144:145], v[110:111], v[104:105] op_sel_hi:[1,0,1]
	v_cvt_pk_f32_fp8_sdwa v[202:203], v203 src0_sel:WORD_1
	v_pk_fma_f32 v[118:119], v[188:189], v[114:115], v[118:119] op_sel_hi:[1,0,1]
	v_pk_fma_f32 v[120:121], v[190:191], v[114:115], v[120:121] op_sel_hi:[1,0,1]
	v_pk_fma_f32 v[122:123], v[192:193], v[114:115], v[122:123] op_sel_hi:[1,0,1]
	v_pk_fma_f32 v[104:105], v[146:147], v[112:113], v[104:105] op_sel_hi:[1,0,1]
	s_waitcnt lgkmcnt(4)
	v_cvt_pk_f32_fp8_e32 v[124:125], v207
	v_pk_fma_f32 v[118:119], v[194:195], v[98:99], v[118:119] op_sel_hi:[1,0,1]
	v_pk_fma_f32 v[120:121], v[196:197], v[98:99], v[120:121] op_sel_hi:[1,0,1]
	v_pk_fma_f32 v[122:123], v[198:199], v[98:99], v[122:123] op_sel_hi:[1,0,1]
	v_pk_fma_f32 v[104:105], v[148:149], v[114:115], v[104:105] op_sel_hi:[1,0,1]
	v_pk_fma_f32 v[118:119], v[216:217], v[100:101], v[118:119] op_sel_hi:[1,0,1]
	v_pk_fma_f32 v[120:121], v[218:219], v[100:101], v[120:121] op_sel_hi:[1,0,1]
	v_pk_fma_f32 v[122:123], v[220:221], v[100:101], v[122:123] op_sel_hi:[1,0,1]
	v_pk_fma_f32 v[98:99], v[150:151], v[98:99], v[104:105] op_sel_hi:[1,0,1]
	v_pk_fma_f32 v[118:119], v[222:223], v[102:103], v[118:119] op_sel_hi:[1,0,1]
	v_pk_fma_f32 v[120:121], v[224:225], v[102:103], v[120:121] op_sel_hi:[1,0,1]
	v_pk_fma_f32 v[122:123], v[226:227], v[102:103], v[122:123] op_sel_hi:[1,0,1]
	v_pk_fma_f32 v[98:99], v[200:201], v[100:101], v[98:99] op_sel_hi:[1,0,1]
	v_cvt_pk_f32_fp8_e32 v[106:107], v204
	v_cvt_pk_f32_fp8_sdwa v[108:109], v204 src0_sel:WORD_1
	v_cvt_pk_f32_fp8_e32 v[110:111], v205
	v_cvt_pk_f32_fp8_sdwa v[112:113], v205 src0_sel:WORD_1
	v_cvt_pk_f32_fp8_e32 v[114:115], v206
	v_cvt_pk_f32_fp8_sdwa v[116:117], v206 src0_sel:WORD_1
	v_cvt_pk_f32_fp8_sdwa v[126:127], v207 src0_sel:WORD_1
	s_waitcnt lgkmcnt(3)
	v_cvt_pk_f32_fp8_e32 v[128:129], v208
	v_cvt_pk_f32_fp8_sdwa v[130:131], v208 src0_sel:WORD_1
	v_cvt_pk_f32_fp8_e32 v[132:133], v209
	v_cvt_pk_f32_fp8_sdwa v[134:135], v209 src0_sel:WORD_1
	s_waitcnt lgkmcnt(2)
	v_cvt_pk_f32_fp8_e32 v[136:137], v210
	v_cvt_pk_f32_fp8_sdwa v[138:139], v210 src0_sel:WORD_1
	v_cvt_pk_f32_fp8_e32 v[140:141], v211
	v_cvt_pk_f32_fp8_sdwa v[142:143], v211 src0_sel:WORD_1
	s_waitcnt lgkmcnt(1)
	v_cvt_pk_f32_fp8_e32 v[144:145], v212
	v_cvt_pk_f32_fp8_sdwa v[146:147], v212 src0_sel:WORD_1
	v_cvt_pk_f32_fp8_e32 v[148:149], v213
	v_cvt_pk_f32_fp8_sdwa v[152:153], v213 src0_sel:WORD_1
	s_waitcnt lgkmcnt(0)
	v_cvt_pk_f32_fp8_e32 v[154:155], v214
	v_cvt_pk_f32_fp8_sdwa v[156:157], v214 src0_sel:WORD_1
	v_cvt_pk_f32_fp8_e32 v[158:159], v215
	v_cvt_pk_f32_fp8_sdwa v[160:161], v215 src0_sel:WORD_1
	v_pk_fma_f32 v[98:99], v[202:203], v[102:103], v[98:99] op_sel_hi:[1,0,1]
	s_setprio 0
	s_waitcnt vmcnt(40)
	v_and_b32_e32 v9, 0x1fff8, v90
	v_and_b32_e32 v11, 0x1fff8, v92
	v_and_b32_e32 v13, 0x1fff8, v94
	v_and_b32_e32 v15, 0x1fff8, v96
	ds_read_b64 v[100:101], v9
	ds_read_b64 v[102:103], v11
	ds_read_b64 v[104:105], v13
	ds_read_b64 v[150:151], v15
	v_and_b32_e32 v9, 0x1fff8, v76
	v_and_b32_e32 v11, 0x1fff8, v77
	v_and_b32_e32 v13, 0x1fff8, v56
	v_and_b32_e32 v15, 0x1fff8, v57
	ds_read_b64 v[162:163], v9
	ds_read_b64 v[164:165], v11
	ds_read_b64 v[166:167], v13
	ds_read_b64 v[168:169], v15
	s_setprio 1
	v_pk_fma_f32 v[106:107], v[106:107], v[78:79], v[118:119] op_sel_hi:[1,0,1]
	v_pk_fma_f32 v[108:109], v[108:109], v[78:79], v[120:121] op_sel_hi:[1,0,1]
	v_pk_fma_f32 v[110:111], v[110:111], v[78:79], v[122:123] op_sel_hi:[1,0,1]
	v_pk_fma_f32 v[78:79], v[112:113], v[78:79], v[98:99] op_sel_hi:[1,0,1]
	v_pk_fma_f32 v[106:107], v[114:115], v[80:81], v[106:107] op_sel_hi:[1,0,1]
	v_pk_fma_f32 v[108:109], v[116:117], v[80:81], v[108:109] op_sel_hi:[1,0,1]
	v_pk_fma_f32 v[110:111], v[124:125], v[80:81], v[110:111] op_sel_hi:[1,0,1]
	v_pk_fma_f32 v[78:79], v[126:127], v[80:81], v[78:79] op_sel_hi:[1,0,1]
	s_waitcnt lgkmcnt(7)
	v_cvt_pk_f32_fp8_e32 v[170:171], v100
	v_cvt_pk_f32_fp8_sdwa v[172:173], v100 src0_sel:WORD_1
	v_cvt_pk_f32_fp8_e32 v[174:175], v101
	v_cvt_pk_f32_fp8_sdwa v[100:101], v101 src0_sel:WORD_1
	v_pk_fma_f32 v[106:107], v[128:129], v[82:83], v[106:107] op_sel_hi:[1,0,1]
	v_pk_fma_f32 v[108:109], v[130:131], v[82:83], v[108:109] op_sel_hi:[1,0,1]
	v_pk_fma_f32 v[110:111], v[132:133], v[82:83], v[110:111] op_sel_hi:[1,0,1]
	v_pk_fma_f32 v[78:79], v[134:135], v[82:83], v[78:79] op_sel_hi:[1,0,1]
	s_waitcnt lgkmcnt(6)
	v_cvt_pk_f32_fp8_e32 v[176:177], v102
	v_cvt_pk_f32_fp8_sdwa v[178:179], v102 src0_sel:WORD_1
	v_cvt_pk_f32_fp8_e32 v[180:181], v103
	v_cvt_pk_f32_fp8_sdwa v[102:103], v103 src0_sel:WORD_1
	v_pk_fma_f32 v[106:107], v[136:137], v[84:85], v[106:107] op_sel_hi:[1,0,1]
	v_pk_fma_f32 v[108:109], v[138:139], v[84:85], v[108:109] op_sel_hi:[1,0,1]
	v_pk_fma_f32 v[110:111], v[140:141], v[84:85], v[110:111] op_sel_hi:[1,0,1]
	v_pk_fma_f32 v[78:79], v[142:143], v[84:85], v[78:79] op_sel_hi:[1,0,1]
	s_waitcnt lgkmcnt(5)
	v_cvt_pk_f32_fp8_e32 v[182:183], v104
	v_cvt_pk_f32_fp8_sdwa v[184:185], v104 src0_sel:WORD_1
	v_cvt_pk_f32_fp8_e32 v[186:187], v105
	v_cvt_pk_f32_fp8_sdwa v[104:105], v105 src0_sel:WORD_1
	v_pk_fma_f32 v[106:107], v[144:145], v[86:87], v[106:107] op_sel_hi:[1,0,1]
	v_pk_fma_f32 v[108:109], v[146:147], v[86:87], v[108:109] op_sel_hi:[1,0,1]
	v_pk_fma_f32 v[110:111], v[148:149], v[86:87], v[110:111] op_sel_hi:[1,0,1]
	v_pk_fma_f32 v[78:79], v[152:153], v[86:87], v[78:79] op_sel_hi:[1,0,1]
	v_pk_fma_f32 v[106:107], v[154:155], v[88:89], v[106:107] op_sel_hi:[1,0,1]
	v_pk_fma_f32 v[108:109], v[156:157], v[88:89], v[108:109] op_sel_hi:[1,0,1]
	v_pk_fma_f32 v[110:111], v[158:159], v[88:89], v[110:111] op_sel_hi:[1,0,1]
	v_pk_fma_f32 v[78:79], v[160:161], v[88:89], v[78:79] op_sel_hi:[1,0,1]
	s_waitcnt lgkmcnt(3)
	v_cvt_pk_f32_fp8_e32 v[194:195], v162
	v_cvt_pk_f32_fp8_sdwa v[196:197], v162 src0_sel:WORD_1
	v_cvt_pk_f32_fp8_e32 v[198:199], v163
	v_cvt_pk_f32_fp8_sdwa v[162:163], v163 src0_sel:WORD_1
	s_waitcnt lgkmcnt(2)
	v_cvt_pk_f32_fp8_e32 v[200:201], v164
	v_cvt_pk_f32_fp8_sdwa v[202:203], v164 src0_sel:WORD_1
	v_cvt_pk_f32_fp8_e32 v[204:205], v165
	v_cvt_pk_f32_fp8_sdwa v[164:165], v165 src0_sel:WORD_1
	v_pk_fma_f32 v[106:107], v[170:171], v[90:91], v[106:107] op_sel_hi:[1,0,1]
	v_pk_fma_f32 v[108:109], v[172:173], v[90:91], v[108:109] op_sel_hi:[1,0,1]
	v_pk_fma_f32 v[110:111], v[174:175], v[90:91], v[110:111] op_sel_hi:[1,0,1]
	v_pk_fma_f32 v[78:79], v[100:101], v[90:91], v[78:79] op_sel_hi:[1,0,1]
	v_pk_fma_f32 v[106:107], v[176:177], v[92:93], v[106:107] op_sel_hi:[1,0,1]
	v_pk_fma_f32 v[108:109], v[178:179], v[92:93], v[108:109] op_sel_hi:[1,0,1]
	v_pk_fma_f32 v[110:111], v[180:181], v[92:93], v[110:111] op_sel_hi:[1,0,1]
	v_pk_fma_f32 v[78:79], v[102:103], v[92:93], v[78:79] op_sel_hi:[1,0,1]
	v_cvt_pk_f32_fp8_e32 v[188:189], v150
	v_cvt_pk_f32_fp8_sdwa v[190:191], v150 src0_sel:WORD_1
	v_cvt_pk_f32_fp8_e32 v[192:193], v151
	v_cvt_pk_f32_fp8_sdwa v[150:151], v151 src0_sel:WORD_1
	v_pk_fma_f32 v[106:107], v[182:183], v[94:95], v[106:107] op_sel_hi:[1,0,1]
	v_pk_fma_f32 v[108:109], v[184:185], v[94:95], v[108:109] op_sel_hi:[1,0,1]
	v_pk_fma_f32 v[110:111], v[186:187], v[94:95], v[110:111] op_sel_hi:[1,0,1]
	v_pk_fma_f32 v[78:79], v[104:105], v[94:95], v[78:79] op_sel_hi:[1,0,1]
	s_waitcnt lgkmcnt(1)
	v_cvt_pk_f32_fp8_sdwa v[88:89], v167 src0_sel:WORD_1
	s_waitcnt lgkmcnt(0)
	v_cvt_pk_f32_fp8_sdwa v[94:95], v169 src0_sel:WORD_1
	v_pk_fma_f32 v[78:79], v[162:163], v[76:77], v[78:79] op_sel_hi:[1,0,1]
	v_pk_fma_f32 v[106:107], v[188:189], v[96:97], v[106:107] op_sel_hi:[1,0,1]
	v_pk_fma_f32 v[108:109], v[190:191], v[96:97], v[108:109] op_sel_hi:[1,0,1]
	v_pk_fma_f32 v[110:111], v[192:193], v[96:97], v[110:111] op_sel_hi:[1,0,1]
	v_pk_fma_f32 v[78:79], v[150:151], v[96:97], v[78:79] op_sel_hi:[1,0,1]
	v_pk_fma_f32 v[78:79], v[88:89], v[56:57], v[78:79] op_sel_hi:[1,0,1]
	v_pk_fma_f32 v[106:107], v[194:195], v[76:77], v[106:107] op_sel_hi:[1,0,1]
	v_pk_fma_f32 v[108:109], v[196:197], v[76:77], v[108:109] op_sel_hi:[1,0,1]
	v_pk_fma_f32 v[110:111], v[198:199], v[76:77], v[110:111] op_sel_hi:[1,0,1]
	v_mov_b32_e32 v76, v77
	v_pk_fma_f32 v[78:79], v[164:165], v[76:77], v[78:79] op_sel:[0,1,0] op_sel_hi:[1,1,1]
	v_cvt_pk_f32_fp8_e32 v[82:83], v166
	v_cvt_pk_f32_fp8_sdwa v[84:85], v166 src0_sel:WORD_1
	v_cvt_pk_f32_fp8_e32 v[86:87], v167
	v_cvt_pk_f32_fp8_e32 v[90:91], v168
	v_cvt_pk_f32_fp8_sdwa v[92:93], v168 src0_sel:WORD_1
	v_cvt_pk_f32_fp8_e32 v[96:97], v169
	v_pk_fma_f32 v[78:79], v[94:95], v[56:57], v[78:79] op_sel:[0,1,0] op_sel_hi:[1,1,1]
	s_setprio 0
	s_waitcnt vmcnt(32)
	v_and_b32_e32 v9, 0x1fff8, v58
	v_and_b32_e32 v11, 0x1fff8, v59
	v_and_b32_e32 v13, 0x1fff8, v60
	v_and_b32_e32 v15, 0x1fff8, v61
	ds_read_b64 v[100:101], v9
	ds_read_b64 v[102:103], v11
	ds_read_b64 v[104:105], v13
	ds_read_b64 v[112:113], v15
	v_and_b32_e32 v9, 0x1fff8, v62
	v_and_b32_e32 v11, 0x1fff8, v63
	v_and_b32_e32 v13, 0x1fff8, v54
	v_and_b32_e32 v15, 0x1fff8, v55
	ds_read_b64 v[114:115], v9
	ds_read_b64 v[118:119], v11
	ds_read_b64 v[120:121], v13
	ds_read_b64 v[122:123], v15
	s_setprio 1
	s_waitcnt lgkmcnt(7)
	v_cvt_pk_f32_fp8_e32 v[124:125], v100
	v_cvt_pk_f32_fp8_sdwa v[126:127], v100 src0_sel:WORD_1
	v_cvt_pk_f32_fp8_e32 v[128:129], v101
	v_cvt_pk_f32_fp8_sdwa v[100:101], v101 src0_sel:WORD_1
	s_waitcnt lgkmcnt(6)
	v_cvt_pk_f32_fp8_sdwa v[134:135], v103 src0_sel:WORD_1
	v_cvt_pk_f32_fp8_e32 v[130:131], v102
	s_waitcnt lgkmcnt(5)
	v_cvt_pk_f32_fp8_e32 v[138:139], v104
	v_cvt_pk_f32_fp8_sdwa v[140:141], v104 src0_sel:WORD_1
	v_cvt_pk_f32_fp8_e32 v[142:143], v105
	v_cvt_pk_f32_fp8_sdwa v[104:105], v105 src0_sel:WORD_1
	s_waitcnt lgkmcnt(4)
	v_cvt_pk_f32_fp8_sdwa v[148:149], v113 src0_sel:WORD_1
	v_pk_fma_f32 v[106:107], v[200:201], v[76:77], v[106:107] op_sel_hi:[1,0,1]
	s_waitcnt lgkmcnt(3)
	v_cvt_pk_f32_fp8_e32 v[152:153], v114
	v_cvt_pk_f32_fp8_sdwa v[154:155], v114 src0_sel:WORD_1
	v_cvt_pk_f32_fp8_e32 v[156:157], v115
	v_cvt_pk_f32_fp8_sdwa v[114:115], v115 src0_sel:WORD_1
	s_waitcnt lgkmcnt(2)
	v_cvt_pk_f32_fp8_sdwa v[162:163], v119 src0_sel:WORD_1
	v_pk_fma_f32 v[82:83], v[82:83], v[56:57], v[106:107] op_sel_hi:[1,0,1]
	v_mov_b32_e32 v106, v57
	v_cvt_pk_f32_fp8_e32 v[144:145], v112
	v_cvt_pk_f32_fp8_e32 v[158:159], v118
	v_cvt_pk_f32_fp8_sdwa v[160:161], v118 src0_sel:WORD_1
	v_cvt_pk_f32_fp8_e32 v[164:165], v119
	s_waitcnt lgkmcnt(1)
	v_cvt_pk_f32_fp8_e32 v[118:119], v120
	v_cvt_pk_f32_fp8_sdwa v[168:169], v120 src0_sel:WORD_1
	v_cvt_pk_f32_fp8_e32 v[170:171], v121
	v_cvt_pk_f32_fp8_sdwa v[120:121], v121 src0_sel:WORD_1
	s_waitcnt lgkmcnt(0)
; #define GAS __attribute__((address_space(1)))
; __device__ __forceinline__ unsigned f2bf(float f) { unsigned u = __builtin_bit_cast(unsigned, f); return (u + 0x7fffu + ((u >> 16) & 1u)) >> 16; }
; template <int VVAR> __device__ __forceinline__ void peer_v_phase(LAS unsigned char* lds, int wave, int vcu, const unsigned char* __restrict__ VS_l, const unsigned* __restrict__ PW, bf16* __restrict__ Y) {
;     ...
; #pragma unroll 1
;     for (int it = 0; it < (VVAR == 5 ? 2 : 64); it += 2) {
;         V_HALF(pa, pb, it + 1);
;         V_HALF(pb, pa, it + 2);
;         if ((it & 3) == 2) {
;             const int blk = th * 128 + wave + 8 * (it >> 2);
;             bf16* yp = Y + ((size_t)blk * 1024 + cs * 8) * 64 + lane;
; #pragma unroll
;             for (int c = 0; c < 8; ++c) ((GAS unsigned short*)yp)[c * 64] = (unsigned short)f2bf(acc[c]);
; #pragma unroll
;             for (int c = 0; c < 8; ++c) acc[c] = 0.f;
	v_cvt_pk_f32_fp8_sdwa v[176:177], v123 src0_sel:WORD_1
	v_pk_fma_f32 v[82:83], v[90:91], v[106:107], v[82:83] op_sel_hi:[1,0,1]
	v_pk_fma_f32 v[78:79], v[100:101], v[58:59], v[78:79] op_sel_hi:[1,0,1]
	v_pk_fma_f32 v[78:79], v[134:135], v[58:59], v[78:79] op_sel:[0,1,0] op_sel_hi:[1,1,1]
	v_pk_fma_f32 v[82:83], v[124:125], v[58:59], v[82:83] op_sel_hi:[1,0,1]
	v_mov_b32_e32 v90, v59
	v_pk_fma_f32 v[78:79], v[104:105], v[60:61], v[78:79] op_sel_hi:[1,0,1]
	v_pk_fma_f32 v[78:79], v[148:149], v[60:61], v[78:79] op_sel:[0,1,0] op_sel_hi:[1,1,1]
	v_pk_fma_f32 v[82:83], v[130:131], v[90:91], v[82:83] op_sel_hi:[1,0,1]
	v_pk_fma_f32 v[78:79], v[114:115], v[62:63], v[78:79] op_sel_hi:[1,0,1]
	v_pk_fma_f32 v[78:79], v[162:163], v[62:63], v[78:79] op_sel:[0,1,0] op_sel_hi:[1,1,1]
	v_pk_fma_f32 v[82:83], v[138:139], v[60:61], v[82:83] op_sel_hi:[1,0,1]
	v_mov_b32_e32 v116, v61
	v_cvt_pk_f32_fp8_e32 v[172:173], v122
	v_pk_fma_f32 v[78:79], v[120:121], v[54:55], v[78:79] op_sel_hi:[1,0,1]
	v_pk_fma_f32 v[82:83], v[144:145], v[116:117], v[82:83] op_sel_hi:[1,0,1]
	v_pk_fma_f32 v[78:79], v[176:177], v[54:55], v[78:79] op_sel:[0,1,0] op_sel_hi:[1,1,1]
	v_pk_fma_f32 v[82:83], v[152:153], v[62:63], v[82:83] op_sel_hi:[1,0,1]
	v_mov_b32_e32 v120, v63
	v_pk_fma_f32 v[82:83], v[158:159], v[120:121], v[82:83] op_sel_hi:[1,0,1]
	v_mov_b32_e32 v124, v55
	v_pk_fma_f32 v[82:83], v[118:119], v[54:55], v[82:83] op_sel_hi:[1,0,1]
	v_cvt_pk_f32_fp8_sdwa v[132:133], v102 src0_sel:WORD_1
	v_cvt_pk_f32_fp8_e32 v[102:103], v103
	v_pk_fma_f32 v[118:119], v[172:173], v[124:125], v[82:83] op_sel_hi:[1,0,1]
	v_pk_fma_f32 v[82:83], v[202:203], v[76:77], v[108:109] op_sel_hi:[1,0,1]
	v_pk_fma_f32 v[76:77], v[204:205], v[76:77], v[110:111] op_sel_hi:[1,0,1]
	v_pk_fma_f32 v[82:83], v[84:85], v[56:57], v[82:83] op_sel_hi:[1,0,1]
	v_pk_fma_f32 v[56:57], v[86:87], v[56:57], v[76:77] op_sel_hi:[1,0,1]
	v_cvt_pk_f32_fp8_sdwa v[146:147], v112 src0_sel:WORD_1
	v_cvt_pk_f32_fp8_e32 v[112:113], v113
	v_pk_fma_f32 v[56:57], v[96:97], v[106:107], v[56:57] op_sel_hi:[1,0,1]
	v_pk_fma_f32 v[82:83], v[92:93], v[106:107], v[82:83] op_sel_hi:[1,0,1]
	v_pk_fma_f32 v[56:57], v[128:129], v[58:59], v[56:57] op_sel_hi:[1,0,1]
	v_pk_fma_f32 v[82:83], v[126:127], v[58:59], v[82:83] op_sel_hi:[1,0,1]
	v_pk_fma_f32 v[56:57], v[102:103], v[90:91], v[56:57] op_sel_hi:[1,0,1]
	v_cvt_pk_f32_fp8_e32 v[178:179], v123
	v_pk_fma_f32 v[56:57], v[142:143], v[60:61], v[56:57] op_sel_hi:[1,0,1]
	v_pk_fma_f32 v[82:83], v[132:133], v[90:91], v[82:83] op_sel_hi:[1,0,1]
	v_pk_fma_f32 v[56:57], v[112:113], v[116:117], v[56:57] op_sel_hi:[1,0,1]
	v_pk_fma_f32 v[82:83], v[140:141], v[60:61], v[82:83] op_sel_hi:[1,0,1]
	v_pk_fma_f32 v[56:57], v[156:157], v[62:63], v[56:57] op_sel_hi:[1,0,1]
	v_pk_fma_f32 v[82:83], v[146:147], v[116:117], v[82:83] op_sel_hi:[1,0,1]
	v_pk_fma_f32 v[56:57], v[164:165], v[120:121], v[56:57] op_sel_hi:[1,0,1]
	v_pk_fma_f32 v[82:83], v[154:155], v[62:63], v[82:83] op_sel_hi:[1,0,1]
	v_pk_fma_f32 v[56:57], v[170:171], v[54:55], v[56:57] op_sel_hi:[1,0,1]
	v_pk_fma_f32 v[82:83], v[160:161], v[120:121], v[82:83] op_sel_hi:[1,0,1]
	v_pk_fma_f32 v[120:121], v[178:179], v[124:125], v[56:57] op_sel_hi:[1,0,1]
	v_cvt_pk_f32_fp8_sdwa v[174:175], v122 src0_sel:WORD_1
	v_pk_fma_f32 v[82:83], v[168:169], v[54:55], v[82:83] op_sel_hi:[1,0,1]
	v_pk_fma_f32 v[122:123], v[174:175], v[124:125], v[82:83] op_sel_hi:[1,0,1]
	v_mov_b32_e32 v124, v78
	v_mov_b32_e32 v125, v79
	s_setprio 0
	s_bitcmp0_b32 s17, 1
	s_cbranch_scc1 .LBB0_955
	s_lshl_b64 s[8:9], s[8:9], 17
	v_bfe_u32 v9, v118, 16, 1
	v_lshl_add_u64 v[54:55], v[0:1], 0, s[8:9]
	v_add3_u32 v9, v118, v9, s15
	global_store_short_d16_hi v[54:55], v9, off
	v_bfe_u32 v9, v119, 16, 1
	v_add3_u32 v9, v119, v9, s15
	global_store_short_d16_hi v[54:55], v9, off offset:128
	v_bfe_u32 v9, v122, 16, 1
	v_add3_u32 v9, v122, v9, s15
	global_store_short_d16_hi v[54:55], v9, off offset:256
	v_bfe_u32 v9, v123, 16, 1
	v_add3_u32 v9, v123, v9, s15
	global_store_short_d16_hi v[54:55], v9, off offset:384
	v_bfe_u32 v9, v120, 16, 1
	v_add3_u32 v9, v120, v9, s15
	global_store_short_d16_hi v[54:55], v9, off offset:512
	v_bfe_u32 v9, v121, 16, 1
	v_add3_u32 v9, v121, v9, s15
	global_store_short_d16_hi v[54:55], v9, off offset:640
	v_bfe_u32 v9, v124, 16, 1
	v_add3_u32 v9, v124, v9, s15
	global_store_short_d16_hi v[54:55], v9, off offset:768
	v_bfe_u32 v9, v125, 16, 1
	v_mov_b32_e32 v118, 0
	v_add3_u32 v9, v125, v9, s15
	v_mov_b32_e32 v119, v118
	v_mov_b32_e32 v122, v118
	v_mov_b32_e32 v123, v118
	v_mov_b32_e32 v120, v118
	v_mov_b32_e32 v121, v118
	v_mov_b32_e32 v124, v118
	v_mov_b32_e32 v125, v118
	global_store_short_d16_hi v[54:55], v9, off offset:896
	s_branch .LBB0_955
